# mixer-A bias-table reads hoisted to the step top (16 ds_read2 into own registers) combined with the softmax VALU diet
# baseline (speedup 1.0000x reference)
.LBB0_806:
	s_min_u32 s8, s7, 8
	s_add_i32 s8, s8, s6
	v_med3_i32 v5, s8, 0, v184
	v_lshl_or_b32 v2, v5, 11, v160
	v_lshl_add_u64 v[94:95], v[172:173], 0, v[2:3]
	v_lshlrev_b32_e32 v2, 12, v5
	v_lshl_add_u64 v[122:123], v[174:175], 0, v[2:3]
	global_load_dwordx4 v[90:93], v[94:95], off
	s_nop 0
	global_load_dwordx4 v[94:97], v[94:95], off offset:1024
	s_nop 0
	global_load_dwordx4 v[106:109], v[122:123], off
	global_load_dwordx4 v[110:113], v[122:123], off offset:1024
	global_load_dwordx4 v[118:121], v[122:123], off offset:2048
	s_nop 0
	global_load_dwordx4 v[122:125], v[122:123], off offset:3072
	s_add_i32 s8, s6, s7
	s_add_i32 s8, s8, -1
	s_cmpk_gt_u32 s8, 0xff
	s_cbranch_scc1 .LBB0_816
	ds_read2_b32 v[214:215], v190 offset1:1
	ds_read2_b32 v[216:217], v190 offset0:2 offset1:3
	ds_read2_b32 v[218:219], v190 offset0:16 offset1:17
	ds_read2_b32 v[220:221], v190 offset0:18 offset1:19
	v_add_u32_e32 v246, 0x504, v190
	v_add_u32_e32 v247, 0x50c, v190
	ds_read2_b32 v[222:223], v246 offset1:1
	ds_read2_b32 v[224:225], v247 offset1:1
	v_add_u32_e32 v246, 0x544, v190
	v_add_u32_e32 v247, 0x54c, v190
	ds_read2_b32 v[226:227], v246 offset1:1
	ds_read2_b32 v[228:229], v247 offset1:1
	v_add_u32_e32 v246, 0xa08, v190
	v_add_u32_e32 v247, 0xa10, v190
	ds_read2_b32 v[230:231], v246 offset1:1
	ds_read2_b32 v[232:233], v247 offset1:1
	v_add_u32_e32 v246, 0xa48, v190
	v_add_u32_e32 v247, 0xa50, v190
	ds_read2_b32 v[234:235], v246 offset1:1
	ds_read2_b32 v[236:237], v247 offset1:1
	v_add_u32_e32 v246, 0xf0c, v190
	v_add_u32_e32 v247, 0xf14, v190
	ds_read2_b32 v[238:239], v246 offset1:1
	ds_read2_b32 v[240:241], v247 offset1:1
	v_add_u32_e32 v246, 0xf4c, v190
	v_add_u32_e32 v247, 0xf54, v190
	ds_read2_b32 v[242:243], v246 offset1:1
	ds_read2_b32 v[244:245], v247 offset1:1
	s_waitcnt vmcnt(11) lgkmcnt(14)
	v_mfma_f32_16x16x32_fp8_fp8 v[134:137], v[130:131], v[70:71], v[214:217]
	v_mfma_f32_16x16x32_fp8_fp8 v[138:141], v[132:133], v[72:73], v[134:137]
	s_waitcnt vmcnt(10) lgkmcnt(12)
	v_mfma_f32_16x16x32_fp8_fp8 v[134:137], v[126:127], v[70:71], v[218:221]
	v_mfma_f32_16x16x32_fp8_fp8 v[134:137], v[128:129], v[72:73], v[134:137]
	s_nop 4
	v_max3_f32 v2, v138, v139, v140
	s_nop 1
	v_max3_f32 v191, v141, v134, v135
	v_max3_f32 v2, v2, v136, v137
	v_max_f32_e32 v2, v2, v191
	v_mov_b32_e32 v5, v2
	s_nop 1
	v_permlane16_swap_b32_e32 v2, v5
	v_max_f32_e32 v2, v2, v5
	v_mov_b32_e32 v5, v2
	s_nop 1
	v_permlane32_swap_b32_e32 v2, v5
	v_max_f32_e32 v2, v2, v5
	v_cmp_gt_f32_e32 vcc, v2, v176
	s_cbranch_vccz .LBB0_809
	v_max_f32_e32 v2, v2, v2
	v_max_f32_e32 v5, v176, v176
	v_max_f32_e32 v5, v5, v2
	v_sub_f32_e32 v2, v176, v5
	v_exp_f32_e32 v2, v2
	v_mov_b32_e32 v176, v5
	v_mul_f32_e32 v4, v4, v2
	v_pk_mul_f32 v[68:69], v[68:69], v[2:3] op_sel_hi:[1,0]
	v_pk_mul_f32 v[66:67], v[66:67], v[2:3] op_sel_hi:[1,0]
	v_pk_mul_f32 v[64:65], v[64:65], v[2:3] op_sel_hi:[1,0]
	v_pk_mul_f32 v[62:63], v[62:63], v[2:3] op_sel_hi:[1,0]
	v_pk_mul_f32 v[60:61], v[60:61], v[2:3] op_sel_hi:[1,0]
	v_pk_mul_f32 v[58:59], v[58:59], v[2:3] op_sel_hi:[1,0]
	v_pk_mul_f32 v[56:57], v[56:57], v[2:3] op_sel_hi:[1,0]
	v_pk_mul_f32 v[54:55], v[54:55], v[2:3] op_sel_hi:[1,0]
.LBB0_809:
	v_sub_f32_e32 v134, v134, v176
	v_exp_f32_e32 v193, v134
	v_sub_f32_e32 v134, v135, v176
	v_sub_f32_e32 v2, v138, v176
	v_sub_f32_e32 v138, v140, v176
	v_exp_f32_e32 v194, v134
	v_sub_f32_e32 v134, v136, v176
	v_sub_f32_e32 v5, v139, v176
	v_exp_f32_e32 v191, v138
	v_sub_f32_e32 v138, v141, v176
	v_exp_f32_e32 v195, v134
	v_sub_f32_e32 v134, v137, v176
	v_exp_f32_e32 v2, v2
	v_exp_f32_e32 v5, v5
	v_exp_f32_e32 v192, v138
	v_exp_f32_e32 v196, v134
	v_cvt_pk_bf16_f32 v136, v193, v194
	v_cvt_pk_bf16_f32 v134, v2, v5
	v_cvt_pk_bf16_f32 v135, v191, v192
	v_cvt_pk_bf16_f32 v137, v195, v196
	s_waitcnt vmcnt(9)
	s_nop 0
	v_mfma_f32_16x16x32_bf16 v[66:69], v[114:117], v[134:137], v[66:69]
	s_waitcnt vmcnt(8)
	v_mfma_f32_16x16x32_bf16 v[62:65], v[102:105], v[134:137], v[62:65]
	s_waitcnt vmcnt(7)
	v_mfma_f32_16x16x32_bf16 v[58:61], v[98:101], v[134:137], v[58:61]
	s_waitcnt vmcnt(6)
	v_mfma_f32_16x16x32_bf16 v[54:57], v[86:89], v[134:137], v[54:57]
	s_waitcnt lgkmcnt(0)
	v_mfma_f32_16x16x32_fp8_fp8 v[134:137], v[130:131], v[74:75], v[222:225]
	v_mfma_f32_16x16x32_fp8_fp8 v[138:141], v[132:133], v[76:77], v[134:137]
	v_mfma_f32_16x16x32_fp8_fp8 v[134:137], v[126:127], v[74:75], v[226:229]
	v_mfma_f32_16x16x32_fp8_fp8 v[134:137], v[128:129], v[76:77], v[134:137]
	s_nop 4
	v_max3_f32 v197, v138, v139, v140
	s_nop 1
	v_max3_f32 v199, v141, v134, v135
	v_max3_f32 v197, v197, v136, v137
	v_max_f32_e32 v197, v197, v199
	v_mov_b32_e32 v198, v197
	s_nop 1
	v_permlane16_swap_b32_e32 v197, v198
	v_max_f32_e32 v197, v197, v198
	v_mov_b32_e32 v198, v197
	s_nop 1
	v_permlane32_swap_b32_e32 v197, v198
	v_max_f32_e32 v197, v197, v198
	v_cmp_gt_f32_e32 vcc, v197, v177
	s_cbranch_vccz .LBB0_811
	v_max_f32_e32 v197, v197, v197
	v_max_f32_e32 v198, v177, v177
	v_max_f32_e32 v197, v198, v197
	v_sub_f32_e32 v177, v177, v197
	v_exp_f32_e32 v198, v177
	v_mov_b32_e32 v177, v197
	v_mul_f32_e32 v189, v189, v198
	v_pk_mul_f32 v[52:53], v[52:53], v[198:199] op_sel_hi:[1,0]
	v_pk_mul_f32 v[50:51], v[50:51], v[198:199] op_sel_hi:[1,0]
	v_pk_mul_f32 v[48:49], v[48:49], v[198:199] op_sel_hi:[1,0]
	v_pk_mul_f32 v[46:47], v[46:47], v[198:199] op_sel_hi:[1,0]
	v_pk_mul_f32 v[44:45], v[44:45], v[198:199] op_sel_hi:[1,0]
	v_pk_mul_f32 v[42:43], v[42:43], v[198:199] op_sel_hi:[1,0]
	v_pk_mul_f32 v[40:41], v[40:41], v[198:199] op_sel_hi:[1,0]
	v_pk_mul_f32 v[38:39], v[38:39], v[198:199] op_sel_hi:[1,0]
.LBB0_811:
	v_sub_f32_e32 v138, v138, v177
	v_sub_f32_e32 v134, v134, v177
	v_exp_f32_e32 v197, v138
	v_sub_f32_e32 v138, v139, v177
	v_exp_f32_e32 v201, v134
	v_sub_f32_e32 v134, v135, v177
	v_exp_f32_e32 v198, v138
	v_sub_f32_e32 v138, v140, v177
	v_exp_f32_e32 v202, v134
	v_sub_f32_e32 v134, v136, v177
	v_exp_f32_e32 v199, v138
	v_sub_f32_e32 v138, v141, v177
	v_exp_f32_e32 v203, v134
	v_sub_f32_e32 v134, v137, v177
	v_exp_f32_e32 v200, v138
	v_exp_f32_e32 v204, v134
	v_cvt_pk_bf16_f32 v134, v197, v198
	v_cvt_pk_bf16_f32 v136, v201, v202
	v_cvt_pk_bf16_f32 v135, v199, v200
	v_cvt_pk_bf16_f32 v137, v203, v204
	s_nop 1
	v_mfma_f32_16x16x32_bf16 v[50:53], v[114:117], v[134:137], v[50:53]
	v_mfma_f32_16x16x32_bf16 v[46:49], v[102:105], v[134:137], v[46:49]
	v_mfma_f32_16x16x32_bf16 v[42:45], v[98:101], v[134:137], v[42:45]
	v_mfma_f32_16x16x32_bf16 v[38:41], v[86:89], v[134:137], v[38:41]
	v_mfma_f32_16x16x32_fp8_fp8 v[134:137], v[130:131], v[78:79], v[230:233]
	v_mfma_f32_16x16x32_fp8_fp8 v[138:141], v[132:133], v[80:81], v[134:137]
	v_mfma_f32_16x16x32_fp8_fp8 v[134:137], v[126:127], v[78:79], v[234:237]
	v_mfma_f32_16x16x32_fp8_fp8 v[134:137], v[128:129], v[80:81], v[134:137]
	s_nop 4
	v_max3_f32 v205, v138, v139, v140
	s_nop 1
	v_max3_f32 v207, v141, v134, v135
	v_max3_f32 v205, v205, v136, v137
	v_max_f32_e32 v205, v205, v207
	v_mov_b32_e32 v206, v205
	s_nop 1
	v_permlane16_swap_b32_e32 v205, v206
	v_max_f32_e32 v205, v205, v206
	v_mov_b32_e32 v206, v205
	s_nop 1
	v_permlane32_swap_b32_e32 v205, v206
	v_max_f32_e32 v205, v205, v206
	v_cmp_gt_f32_e32 vcc, v205, v178
	s_cbranch_vccz .LBB0_813
	v_max_f32_e32 v205, v205, v205
	v_max_f32_e32 v206, v178, v178
	v_max_f32_e32 v205, v206, v205
	v_sub_f32_e32 v178, v178, v205
	v_exp_f32_e32 v178, v178
	s_nop 0
	v_mul_f32_e32 v188, v188, v178
	v_pk_mul_f32 v[36:37], v[36:37], v[178:179] op_sel_hi:[1,0]
	v_pk_mul_f32 v[34:35], v[34:35], v[178:179] op_sel_hi:[1,0]
	v_pk_mul_f32 v[32:33], v[32:33], v[178:179] op_sel_hi:[1,0]
	v_pk_mul_f32 v[30:31], v[30:31], v[178:179] op_sel_hi:[1,0]
	v_pk_mul_f32 v[28:29], v[28:29], v[178:179] op_sel_hi:[1,0]
	v_pk_mul_f32 v[26:27], v[26:27], v[178:179] op_sel_hi:[1,0]
	v_pk_mul_f32 v[24:25], v[24:25], v[178:179] op_sel_hi:[1,0]
	v_pk_mul_f32 v[22:23], v[22:23], v[178:179] op_sel_hi:[1,0]
	v_mov_b32_e32 v178, v205
.LBB0_813:
	v_sub_f32_e32 v138, v138, v178
	v_sub_f32_e32 v139, v139, v178
	v_sub_f32_e32 v140, v140, v178
	v_sub_f32_e32 v141, v141, v178
	v_sub_f32_e32 v134, v134, v178
	v_sub_f32_e32 v135, v135, v178
	v_sub_f32_e32 v136, v136, v178
	v_sub_f32_e32 v137, v137, v178
	v_exp_f32_e32 v138, v138
	v_exp_f32_e32 v139, v139
	v_exp_f32_e32 v140, v140
	v_exp_f32_e32 v141, v141
	v_exp_f32_e32 v134, v134
	v_exp_f32_e32 v135, v135
	v_exp_f32_e32 v136, v136
	v_exp_f32_e32 v137, v137
	v_cvt_pk_bf16_f32 v206, v138, v139
	v_cvt_pk_bf16_f32 v207, v140, v141
	v_cvt_pk_bf16_f32 v208, v134, v135
	v_cvt_pk_bf16_f32 v209, v136, v137
	s_nop 1
	v_mfma_f32_16x16x32_bf16 v[34:37], v[114:117], v[206:209], v[34:37]
	v_mfma_f32_16x16x32_bf16 v[30:33], v[102:105], v[206:209], v[30:33]
	v_mfma_f32_16x16x32_bf16 v[26:29], v[98:101], v[206:209], v[26:29]
	v_mfma_f32_16x16x32_bf16 v[22:25], v[86:89], v[206:209], v[22:25]
	v_mfma_f32_16x16x32_fp8_fp8 v[206:209], v[130:131], v[82:83], v[238:241]
	v_mfma_f32_16x16x32_fp8_fp8 v[210:213], v[126:127], v[82:83], v[242:245]
	v_mfma_f32_16x16x32_fp8_fp8 v[130:133], v[132:133], v[84:85], v[206:209]
	v_mfma_f32_16x16x32_fp8_fp8 v[126:129], v[128:129], v[84:85], v[210:213]
	s_nop 6
	v_max_f32_e32 v205, v131, v131
	v_max_f32_e32 v206, v130, v130
	v_max_f32_e32 v207, v133, v133
	v_max_f32_e32 v205, v206, v205
	v_max_f32_e32 v206, v132, v132
	v_max_f32_e32 v206, v206, v207
	v_max_f32_e32 v207, v129, v129
	v_max_f32_e32 v208, v128, v128
	v_max_f32_e32 v207, v208, v207
	v_max3_f32 v207, v126, v127, v207
	v_max3_f32 v205, v205, v206, v207
	v_mov_b32_e32 v206, v205
	s_nop 1
	v_permlane16_swap_b32_e32 v205, v206
	v_max_f32_e32 v205, v205, v206
	v_mov_b32_e32 v206, v205
	s_nop 1
	v_permlane32_swap_b32_e32 v205, v206
	v_max_f32_e32 v205, v205, v206
	v_cmp_gt_f32_e32 vcc, v205, v179
	s_cbranch_vccz .LBB0_815
	v_max_f32_e32 v205, v205, v205
	v_max_f32_e32 v206, v179, v179
	v_max_f32_e32 v205, v206, v205
	v_sub_f32_e32 v179, v179, v205
	v_exp_f32_e32 v206, v179
	v_mov_b32_e32 v179, v205
	v_mul_f32_e32 v187, v187, v206
	v_pk_mul_f32 v[20:21], v[20:21], v[206:207] op_sel_hi:[1,0]
	v_pk_mul_f32 v[18:19], v[18:19], v[206:207] op_sel_hi:[1,0]
	v_pk_mul_f32 v[16:17], v[16:17], v[206:207] op_sel_hi:[1,0]
	v_pk_mul_f32 v[14:15], v[14:15], v[206:207] op_sel_hi:[1,0]
	v_pk_mul_f32 v[12:13], v[12:13], v[206:207] op_sel_hi:[1,0]
	v_pk_mul_f32 v[10:11], v[10:11], v[206:207] op_sel_hi:[1,0]
	v_pk_mul_f32 v[8:9], v[8:9], v[206:207] op_sel_hi:[1,0]
	v_pk_mul_f32 v[6:7], v[6:7], v[206:207] op_sel_hi:[1,0]
